# attention steady loop loop-edge edit: slot rotation SALU and next V address moved in front of the closing barriers
# speedup vs baseline: 1.0027x; 1.0027x over previous
; #define WAIT_BAR(N) asm volatile("s_waitcnt vmcnt(" #N ") lgkmcnt(0)\n\ts_barrier":::"memory")
;   #define RESC() do{ if(resc){ asm volatile("s_waitcnt lgkmcnt(0)":::"memory"); \
;       _Pragma("unroll") for(int d_=0;d_<2;++d_) _Pragma("unroll") for(int r=0;r<16;++r)o[d_][r]*=wsf[crow(r,hi)]; } }while(0)
;   #define ROT() do{sl_prev=sl_cur;sl_cur=sl_next;sl_next=(sl_next==(NSLOT-1)*SLOTB)?0:sl_next+SLOTB;}while(0)
; template<int THRL> __device__ __forceinline__ void attn_unit(const AttU&U,const bf16*Q,const bf16*__restrict__ K,const bf16*__restrict__ V,bf16*O,char*shm){
;     ...
;   int t=1;
;     ...
;   const int tend=__builtin_amdgcn_readfirstlane((NT-5)<(NT-nband-1)?(NT-5):(NT-nband-1));
;   for(;t<tend;t+=2){
;     STEP(pB0,pB1,pA0,pA1,t,true,true,true);     WAIT_BAR(2); RESC(); ROT();
;     STEP(pA0,pA1,pB0,pB1,t+1,true,true,true);   WAIT_BAR(2); RESC(); ROT();
;   }
.LBB0_917:
	s_waitcnt lgkmcnt(14)
	v_mfma_f32_32x32x16_bf16 v[18:33], v[142:145], v[178:181], v[18:33]
	v_exp_f32_e32 v98, v98
	v_exp_f32_e32 v99, v99
	v_exp_f32_e32 v100, v100
	v_exp_f32_e32 v101, v101
	s_waitcnt lgkmcnt(12)
	v_mfma_f32_32x32x16_bf16 v[2:17], v[142:145], v[174:177], v[2:17]
	v_exp_f32_e32 v102, v102
	v_exp_f32_e32 v103, v103
	v_exp_f32_e32 v104, v104
	v_exp_f32_e32 v105, v105
	v_add_u32_e32 v78, s5, v214
	ds_read_b128 v[62:65], v78
	ds_read_b128 v[174:177], v78 offset:512
	s_waitcnt lgkmcnt(12)
	v_mfma_f32_32x32x16_bf16 v[18:33], v[134:137], v[66:69], v[18:33]
	v_exp_f32_e32 v106, v106
	v_exp_f32_e32 v107, v107
	v_exp_f32_e32 v108, v108
	v_exp_f32_e32 v109, v109
	ds_read_b128 v[178:181], v78 offset:2048
	ds_read_b128 v[170:173], v78 offset:2560
	s_waitcnt lgkmcnt(12)
	v_mfma_f32_32x32x16_bf16 v[2:17], v[134:137], v[70:73], v[2:17]
	v_exp_f32_e32 v110, v110
	v_exp_f32_e32 v111, v111
	v_exp_f32_e32 v112, v112
	v_exp_f32_e32 v113, v113
	ds_read_b128 v[166:169], v78 offset:4096
	ds_read_b128 v[162:165], v78 offset:4608
	s_waitcnt lgkmcnt(12)
	v_mfma_f32_32x32x16_bf16 v[18:33], v[126:129], v[74:77], v[18:33]
	v_exp_f32_e32 v82, v82
	v_exp_f32_e32 v83, v83
	v_exp_f32_e32 v84, v84
	v_exp_f32_e32 v85, v85
	ds_read_b128 v[158:161], v78 offset:6144
	ds_read_b128 v[154:157], v78 offset:6656
	s_waitcnt lgkmcnt(12)
	v_mfma_f32_32x32x16_bf16 v[2:17], v[126:129], v[50:53], v[2:17]
	v_exp_f32_e32 v86, v86
	v_exp_f32_e32 v87, v87
	v_exp_f32_e32 v88, v88
	v_exp_f32_e32 v89, v89
	s_waitcnt lgkmcnt(10)
	v_mfma_f32_32x32x16_bf16 v[18:33], v[122:125], v[54:57], v[18:33]
	v_exp_f32_e32 v90, v90
	v_exp_f32_e32 v91, v91
	v_exp_f32_e32 v92, v92
	v_exp_f32_e32 v93, v93
	s_waitcnt lgkmcnt(8)
	v_mfma_f32_32x32x16_bf16 v[2:17], v[122:125], v[58:61], v[2:17]
	v_exp_f32_e32 v94, v94
	v_exp_f32_e32 v95, v95
	v_exp_f32_e32 v96, v96
	v_exp_f32_e32 v97, v97
	s_andn2_b64 vcc, exec, s[0:1]
	s_add_i32 s0, s5, 0x2000
	s_cmpk_lg_i32 s5, 0x4000
	s_cselect_b32 s34, s0, 0
	v_add_u32_e32 v184, s9, v215
	s_waitcnt vmcnt(2) lgkmcnt(0)
	s_barrier
	s_cbranch_vccnz .LBB0_919
	s_waitcnt lgkmcnt(0)
	ds_read_b128 v[50:53], v182 offset:49248
	ds_read_b128 v[54:57], v182 offset:49216
	ds_read_b128 v[58:61], v182 offset:49184
	ds_read_b128 v[66:69], v182 offset:49152
	s_waitcnt lgkmcnt(3)
	v_pk_mul_f32 v[30:31], v[30:31], v[50:51]
	s_waitcnt lgkmcnt(2)
	v_pk_mul_f32 v[26:27], v[26:27], v[54:55]
	s_waitcnt lgkmcnt(1)
	v_pk_mul_f32 v[22:23], v[22:23], v[58:59]
	v_pk_mul_f32 v[32:33], v[32:33], v[52:53]
	v_pk_mul_f32 v[28:29], v[28:29], v[56:57]
	v_pk_mul_f32 v[24:25], v[24:25], v[60:61]
	s_waitcnt lgkmcnt(0)
	v_pk_mul_f32 v[20:21], v[20:21], v[68:69]
	v_pk_mul_f32 v[18:19], v[18:19], v[66:67]
	v_pk_mul_f32 v[14:15], v[14:15], v[50:51]
	v_pk_mul_f32 v[10:11], v[10:11], v[54:55]
	v_pk_mul_f32 v[6:7], v[6:7], v[58:59]
	v_pk_mul_f32 v[16:17], v[16:17], v[52:53]
	v_pk_mul_f32 v[12:13], v[12:13], v[56:57]
	v_pk_mul_f32 v[8:9], v[8:9], v[60:61]
	v_pk_mul_f32 v[4:5], v[4:5], v[68:69]
	v_pk_mul_f32 v[2:3], v[2:3], v[66:67]
.LBB0_919:
	ds_read_b64_tr_b16 v[150:151], v184 offset:24576
	ds_read_b64_tr_b16 v[152:153], v184 offset:25088
	s_waitcnt lgkmcnt(9)
	v_mfma_f32_32x32x16_bf16 v[66:81], v[62:65], v[138:141], v[34:49]
	v_add_f32_e32 v50, v98, v99
	v_add_f32_e32 v50, v100, v50
	v_add_f32_e32 v50, v101, v50
	v_add_f32_e32 v50, v102, v50
	v_add_f32_e32 v50, v103, v50
	v_cvt_pk_bf16_f32 v142, v98, v99
	v_cvt_pk_bf16_f32 v143, v100, v101
	ds_read_b64_tr_b16 v[146:147], v184 offset:28672
	ds_read_b64_tr_b16 v[148:149], v184 offset:29184
	v_add_f32_e32 v50, v104, v50
	v_add_f32_e32 v50, v105, v50
	v_add_f32_e32 v50, v106, v50
	v_add_f32_e32 v122, v107, v50
	s_waitcnt lgkmcnt(10)
	v_mfma_f32_32x32x16_bf16 v[50:65], v[174:177], v[138:141], v[34:49]
	v_cvt_pk_bf16_f32 v144, v102, v103
	v_cvt_pk_bf16_f32 v145, v104, v105
	ds_read_b64_tr_b16 v[98:99], v184 offset:25600
	ds_read_b64_tr_b16 v[100:101], v184 offset:26112
	s_waitcnt lgkmcnt(11)
	v_mfma_f32_32x32x16_bf16 v[66:81], v[178:181], v[130:133], v[66:81]
	v_add_f32_e32 v102, v108, v122
	v_add_f32_e32 v102, v109, v102
	v_add_f32_e32 v102, v110, v102
	v_add_f32_e32 v122, v111, v102
	v_cvt_pk_bf16_f32 v134, v106, v107
	v_cvt_pk_bf16_f32 v135, v108, v109
	ds_read_b64_tr_b16 v[102:103], v184 offset:29696
	ds_read_b64_tr_b16 v[104:105], v184 offset:30208
	s_waitcnt lgkmcnt(12)
	v_mfma_f32_32x32x16_bf16 v[50:65], v[170:173], v[130:133], v[50:65]
	v_add_f32_e32 v106, v112, v122
	v_add_f32_e32 v106, v113, v106
	v_add_f32_e32 v106, v82, v106
	v_add_f32_e32 v122, v83, v106
	v_cvt_pk_bf16_f32 v136, v110, v111
	v_cvt_pk_bf16_f32 v137, v112, v113
	ds_read_b64_tr_b16 v[106:107], v184 offset:26624
	ds_read_b64_tr_b16 v[108:109], v184 offset:27136
	s_waitcnt lgkmcnt(13)
	v_mfma_f32_32x32x16_bf16 v[66:81], v[166:169], v[118:121], v[66:81]
	v_add_f32_e32 v110, v84, v122
	v_add_f32_e32 v110, v85, v110
	v_add_f32_e32 v110, v86, v110
	v_add_f32_e32 v110, v87, v110
	v_cvt_pk_bf16_f32 v126, v82, v83
	v_cvt_pk_bf16_f32 v127, v84, v85
	ds_read_b64_tr_b16 v[82:83], v184 offset:30720
	ds_read_b64_tr_b16 v[84:85], v184 offset:31232
	s_waitcnt lgkmcnt(14)
	v_mfma_f32_32x32x16_bf16 v[50:65], v[162:165], v[118:121], v[50:65]
	v_add_f32_e32 v110, v88, v110
	v_add_f32_e32 v110, v89, v110
	v_add_f32_e32 v110, v90, v110
	v_add_f32_e32 v110, v91, v110
	v_cvt_pk_bf16_f32 v128, v86, v87
	v_cvt_pk_bf16_f32 v129, v88, v89
	ds_read_b64_tr_b16 v[86:87], v184 offset:27648
	ds_read_b64_tr_b16 v[88:89], v184 offset:28160
	s_waitcnt lgkmcnt(14)
; #define WAIT_BAR(N) asm volatile("s_waitcnt vmcnt(" #N ") lgkmcnt(0)\n\ts_barrier":::"memory")
;   #define RESC() do{ if(resc){ asm volatile("s_waitcnt lgkmcnt(0)":::"memory"); \
;       _Pragma("unroll") for(int d_=0;d_<2;++d_) _Pragma("unroll") for(int r=0;r<16;++r)o[d_][r]*=wsf[crow(r,hi)]; } }while(0)
;   #define ROT() do{sl_prev=sl_cur;sl_cur=sl_next;sl_next=(sl_next==(NSLOT-1)*SLOTB)?0:sl_next+SLOTB;}while(0)
; template<int THRL> __device__ __forceinline__ void attn_unit(const AttU&U,const bf16*Q,const bf16*__restrict__ K,const bf16*__restrict__ V,bf16*O,char*shm){
;     ...
;   int t=1;
;     ...
;   const int tend=__builtin_amdgcn_readfirstlane((NT-5)<(NT-nband-1)?(NT-5):(NT-nband-1));
;   for(;t<tend;t+=2){
;     STEP(pB0,pB1,pA0,pA1,t,true,true,true);     WAIT_BAR(2); RESC(); ROT();
;     STEP(pA0,pA1,pB0,pB1,t+1,true,true,true);   WAIT_BAR(2); RESC(); ROT();
;   }
	v_mfma_f32_32x32x16_bf16 v[66:81], v[158:161], v[114:117], v[66:81]
	v_add_f32_e32 v110, v92, v110
	v_add_f32_e32 v110, v93, v110
	v_add_f32_e32 v110, v94, v110
	v_add_f32_e32 v110, v95, v110
	v_cvt_pk_bf16_f32 v122, v90, v91
	v_cvt_pk_bf16_f32 v123, v92, v93
	ds_read_b64_tr_b16 v[90:91], v184 offset:31744
	ds_read_b64_tr_b16 v[92:93], v184 offset:32256
	v_mfma_f32_32x32x16_bf16 v[50:65], v[154:157], v[114:117], v[50:65]
	v_add_f32_e32 v110, v96, v110
	v_add_f32_e32 v110, v97, v110
	v_add_f32_e32 v110, 0, v110
	v_cvt_pk_bf16_f32 v124, v94, v95
	v_cvt_pk_bf16_f32 v125, v96, v97
	s_cmp_lt_u32 s8, s28
	s_cselect_b32 s0, s29, s33
	s_add_i32 s0, s0, s8
	s_ashr_i32 s1, s0, 31
	s_lshl_b64 s[0:1], s[0:1], 15
	v_lshl_add_u64 v[94:95], v[194:195], 0, s[0:1]
	s_add_i32 s0, s5, s30
	s_add_i32 s9, s8, -2
	s_cmp_lt_u32 s9, s28
	s_mov_b32 s1, m0
	s_mov_b32 m0, s0
	s_nop 0
	global_load_lds_dwordx4 v[94:95], off
	s_mov_b32 m0, s1
	s_cselect_b32 s0, s29, s33
	s_add_i32 s0, s9, s0
	s_ashr_i32 s1, s0, 31
	s_lshl_b64 s[0:1], s[0:1], 15
	v_lshl_add_u64 v[94:95], v[196:197], 0, s[0:1]
	s_add_i32 s0, s34, s31
	s_mov_b32 s1, m0
	s_mov_b32 m0, s0
	s_nop 0
	global_load_lds_dwordx4 v[94:95], off
	s_mov_b32 m0, s1
	v_max_f32_e32 v94, v67, v67
	v_max_f32_e32 v95, v66, v66
	v_max_f32_e32 v94, v95, v94
	v_max3_f32 v95, v68, v69, v51
	v_max3_f32 v94, v94, v50, v52
	v_max3_f32 v94, v94, v53, v70
	v_max3_f32 v95, v95, v72, v73
	v_max3_f32 v94, v94, v71, v54
	v_max3_f32 v95, v95, v56, v57
	v_max3_f32 v94, v94, v55, v74
	v_max3_f32 v95, v95, v76, v77
	v_max3_f32 v94, v94, v75, v58
	v_max3_f32 v95, v95, v60, v61
	v_max3_f32 v94, v94, v59, v78
	v_max3_f32 v95, v95, v80, v81
	v_max3_f32 v94, v94, v79, v62
	v_max3_f32 v95, v95, v64, v65
	v_max3_f32 v94, v94, v63, v95
	v_mov_b32_e32 v95, v94
	s_nop 1
	v_permlane32_swap_b32_e32 v94, v95
	v_max_f32_e32 v95, v95, v95
	v_max_f32_e32 v94, v94, v94
	v_max_f32_e32 v94, v94, v95
	v_cmp_lt_f32_e32 vcc, s16, v94
	s_cmp_lg_u64 vcc, 0
	v_add_f32_e32 v217, v183, v110
	s_cselect_b64 s[0:1], -1, 0
	s_cbranch_vccnz .LBB0_927
.LBB0_920:
	s_waitcnt lgkmcnt(14)
	v_mfma_f32_32x32x16_bf16 v[18:33], v[142:145], v[150:153], v[18:33]
	v_exp_f32_e32 v66, v66
	v_exp_f32_e32 v67, v67
	v_exp_f32_e32 v68, v68
	v_exp_f32_e32 v69, v69
	s_waitcnt lgkmcnt(12)
	v_mfma_f32_32x32x16_bf16 v[2:17], v[142:145], v[146:149], v[2:17]
	v_exp_f32_e32 v70, v70
	v_exp_f32_e32 v71, v71
	v_exp_f32_e32 v72, v72
	v_exp_f32_e32 v73, v73
	v_add_u32_e32 v94, s34, v214
	ds_read_b128 v[174:177], v94
	ds_read_b128 v[170:173], v94 offset:512
	s_waitcnt lgkmcnt(12)
	v_mfma_f32_32x32x16_bf16 v[18:33], v[134:137], v[98:101], v[18:33]
	v_exp_f32_e32 v74, v74
	v_exp_f32_e32 v75, v75
	v_exp_f32_e32 v76, v76
	v_exp_f32_e32 v77, v77
	ds_read_b128 v[166:169], v94 offset:2048
	ds_read_b128 v[162:165], v94 offset:2560
	s_waitcnt lgkmcnt(12)
	v_mfma_f32_32x32x16_bf16 v[2:17], v[134:137], v[102:105], v[2:17]
	v_exp_f32_e32 v78, v78
	v_exp_f32_e32 v79, v79
	v_exp_f32_e32 v80, v80
	v_exp_f32_e32 v81, v81
	ds_read_b128 v[158:161], v94 offset:4096
	ds_read_b128 v[154:157], v94 offset:4608
	s_waitcnt lgkmcnt(12)
	v_mfma_f32_32x32x16_bf16 v[18:33], v[126:129], v[106:109], v[18:33]
	v_exp_f32_e32 v50, v50
	v_exp_f32_e32 v51, v51
	v_exp_f32_e32 v52, v52
	v_exp_f32_e32 v53, v53
	ds_read_b128 v[150:153], v94 offset:6144
	ds_read_b128 v[146:149], v94 offset:6656
	s_waitcnt lgkmcnt(12)
	v_mfma_f32_32x32x16_bf16 v[2:17], v[126:129], v[82:85], v[2:17]
	v_exp_f32_e32 v54, v54
	v_exp_f32_e32 v55, v55
	v_exp_f32_e32 v56, v56
	v_exp_f32_e32 v57, v57
	s_waitcnt lgkmcnt(10)
	v_mfma_f32_32x32x16_bf16 v[18:33], v[122:125], v[86:89], v[18:33]
	v_exp_f32_e32 v58, v58
	v_exp_f32_e32 v59, v59
	v_exp_f32_e32 v60, v60
	v_exp_f32_e32 v61, v61
	s_waitcnt lgkmcnt(8)
	v_mfma_f32_32x32x16_bf16 v[2:17], v[122:125], v[90:93], v[2:17]
	v_exp_f32_e32 v62, v62
	v_exp_f32_e32 v63, v63
	v_exp_f32_e32 v64, v64
	v_exp_f32_e32 v65, v65
	s_andn2_b64 vcc, exec, s[0:1]
	s_add_i32 s0, s34, 0x2000
	s_cmpk_lg_i32 s34, 0x4000
	s_cselect_b32 s35, s0, 0
	s_add_i32 s8, s8, 2
	s_waitcnt vmcnt(2) lgkmcnt(0)
	s_barrier
	s_cbranch_vccnz .LBB0_922
	s_waitcnt lgkmcnt(0)
	ds_read_b128 v[82:85], v182 offset:49248
	ds_read_b128 v[86:89], v182 offset:49216
	ds_read_b128 v[90:93], v182 offset:49184
	ds_read_b128 v[94:97], v182 offset:49152
	s_waitcnt lgkmcnt(3)
	v_pk_mul_f32 v[30:31], v[30:31], v[82:83]
	s_waitcnt lgkmcnt(2)
	v_pk_mul_f32 v[26:27], v[26:27], v[86:87]
	s_waitcnt lgkmcnt(1)
	v_pk_mul_f32 v[22:23], v[22:23], v[90:91]
	v_pk_mul_f32 v[32:33], v[32:33], v[84:85]
	v_pk_mul_f32 v[28:29], v[28:29], v[88:89]
	v_pk_mul_f32 v[24:25], v[24:25], v[92:93]
	s_waitcnt lgkmcnt(0)
	v_pk_mul_f32 v[20:21], v[20:21], v[96:97]
	v_pk_mul_f32 v[18:19], v[18:19], v[94:95]
	v_pk_mul_f32 v[14:15], v[14:15], v[82:83]
	v_pk_mul_f32 v[10:11], v[10:11], v[86:87]
	v_pk_mul_f32 v[6:7], v[6:7], v[90:91]
	v_pk_mul_f32 v[16:17], v[16:17], v[84:85]
	v_pk_mul_f32 v[12:13], v[12:13], v[88:89]
	v_pk_mul_f32 v[8:9], v[8:9], v[92:93]
	v_pk_mul_f32 v[4:5], v[4:5], v[96:97]
	v_pk_mul_f32 v[2:3], v[2:3], v[94:95]
.LBB0_922:
	s_cmp_ge_i32 s9, s7
	s_cbranch_scc1 .LBB0_931
	s_mov_b32 s0, s5
	s_mov_b32 s9, s34
	s_mov_b32 s5, s35
	s_branch .LBB0_916
